# v044 + grid barrier: XCD leaders poll the TOP counter (>= target) instead of the TOPGEN word
# speedup vs baseline: 1.0114x; 1.0018x over previous
; __device__ __forceinline__ unsigned xb_ld(unsigned* p)              { return __hip_atomic_load(p, __ATOMIC_RELAXED, __HIP_MEMORY_SCOPE_AGENT); }
; __device__ __forceinline__ unsigned xb_add(unsigned* p, unsigned v) { return __hip_atomic_fetch_add(p, v, __ATOMIC_RELAXED, __HIP_MEMORY_SCOPE_AGENT); }
; #define XB_SPIN(cond, bar) do { unsigned _sp = 0; while (cond) { __builtin_amdgcn_s_sleep(1); \
;     if ((++_sp & 255u) == 0u) { if (xb_ld(&(bar)[XB_TMO])) break; if (_sp > XB_SPIN_CAP) { atomicAdd(&(bar)[XB_TMO], 1u); break; } } } } while (0)
; __device__ __forceinline__ void xcd_barrier(const XcdBarrier& b) {
;     ...
;             const unsigned og = xb_add(&bar[XB_TOP], 1u);
;             const unsigned tg = og / nx;
;             if (og + 1u == (tg + 1u) * nx) xb_add(&bar[XB_TOPGEN], 1u);
;             else XB_SPIN(xb_ld(&bar[XB_TOPGEN]) == tg, bar);
.LBB0_97:
	s_or_b64 exec, exec, s[10:11]
	buffer_inv sc1
	v_cvt_f32_u32_e32 v4, v1
	s_waitcnt vmcnt(0)
	v_readfirstlane_b32 s3, v3
	s_add_u32 s10, s90, 0x3500
	s_addc_u32 s11, s91, 0
	v_rcp_iflag_f32_e32 v4, v4
	v_add_u32_e32 v2, s3, v2
	v_add_u32_e32 v5, 1, v2
	s_mov_b64 s[12:13], -1
	v_mul_f32_e32 v3, 0x4f7ffffe, v4
	v_cvt_u32_f32_e32 v3, v3
	v_sub_u32_e32 v4, 0, v1
	v_mul_lo_u32 v4, v4, v3
	v_mul_hi_u32 v4, v3, v4
	v_add_u32_e32 v3, v3, v4
	v_mul_hi_u32 v3, v2, v3
	v_mul_lo_u32 v4, v3, v1
	v_sub_u32_e32 v2, v2, v4
	v_add_u32_e32 v6, 1, v3
	v_cmp_ge_u32_e32 vcc, v2, v1
	v_sub_u32_e32 v4, v2, v1
	s_nop 0
	v_cndmask_b32_e32 v3, v3, v6, vcc
	v_cndmask_b32_e32 v2, v2, v4, vcc
	v_add_u32_e32 v4, 1, v3
	v_cmp_ge_u32_e32 vcc, v2, v1
	s_nop 1
	v_cndmask_b32_e32 v4, v3, v4, vcc
	v_mul_lo_u32 v2, v1, v4
	v_add_u32_e32 v1, v2, v1
	v_cmp_ne_u32_e32 vcc, v5, v1
	v_mov_b64_e32 v[2:3], s[10:11]
	s_and_saveexec_b64 s[8:9], vcc
	s_cbranch_execz .LBB0_109
	v_mov_b32_e32 v7, v1
	v_mov_b32_e32 v1, 0
	global_load_dword v2, v1, s[10:11] offset:-256 sc1
	s_mov_b64 s[16:17], 0
	s_waitcnt vmcnt(0)
	v_cmp_lt_u32_e32 vcc, v2, v7
	s_and_saveexec_b64 s[14:15], vcc
	s_cbranch_execz .LBB0_108
	s_add_u32 s12, s90, 0x200
	s_addc_u32 s13, s91, 0
	s_mov_b32 s3, 1
	s_branch .LBB0_101

; __device__ __forceinline__ unsigned xb_ld(unsigned* p)              { return __hip_atomic_load(p, __ATOMIC_RELAXED, __HIP_MEMORY_SCOPE_AGENT); }
; __device__ __forceinline__ unsigned xb_add(unsigned* p, unsigned v) { return __hip_atomic_fetch_add(p, v, __ATOMIC_RELAXED, __HIP_MEMORY_SCOPE_AGENT); }
; #define XB_SPIN(cond, bar) do { unsigned _sp = 0; while (cond) { __builtin_amdgcn_s_sleep(1); \
;     if ((++_sp & 255u) == 0u) { if (xb_ld(&(bar)[XB_TMO])) break; if (_sp > XB_SPIN_CAP) { atomicAdd(&(bar)[XB_TMO], 1u); break; } } } } while (0)
; __device__ __forceinline__ void xcd_barrier(const XcdBarrier& b) {
;     ...
;             const unsigned og = xb_add(&bar[XB_TOP], 1u);
;             const unsigned tg = og / nx;
;             if (og + 1u == (tg + 1u) * nx) xb_add(&bar[XB_TOPGEN], 1u);
;             else XB_SPIN(xb_ld(&bar[XB_TOPGEN]) == tg, bar);
.LBB0_103:
	global_load_dword v2, v1, s[10:11] offset:-256 sc1
	s_add_i32 s3, s3, 1
	s_mov_b64 s[20:21], -1
	s_waitcnt vmcnt(0)
	v_cmp_ge_u32_e32 vcc, v2, v7
	s_orn2_b64 s[24:25], vcc, exec
	s_branch .LBB0_100

; __device__ __forceinline__ unsigned xb_ld(unsigned* p)              { return __hip_atomic_load(p, __ATOMIC_RELAXED, __HIP_MEMORY_SCOPE_AGENT); }
; __device__ __forceinline__ unsigned xb_add(unsigned* p, unsigned v) { return __hip_atomic_fetch_add(p, v, __ATOMIC_RELAXED, __HIP_MEMORY_SCOPE_AGENT); }
; #define XB_SPIN(cond, bar) do { unsigned _sp = 0; while (cond) { __builtin_amdgcn_s_sleep(1); \
;     if ((++_sp & 255u) == 0u) { if (xb_ld(&(bar)[XB_TMO])) break; if (_sp > XB_SPIN_CAP) { atomicAdd(&(bar)[XB_TMO], 1u); break; } } } } while (0)
; __device__ __forceinline__ void xcd_barrier(const XcdBarrier& b) {
;     ...
;             const unsigned og = xb_add(&bar[XB_TOP], 1u);
;             const unsigned tg = og / nx;
;             if (og + 1u == (tg + 1u) * nx) xb_add(&bar[XB_TOPGEN], 1u);
;             else XB_SPIN(xb_ld(&bar[XB_TOPGEN]) == tg, bar);
.LBB0_158:
	s_or_b64 exec, exec, s[6:7]
	buffer_inv sc1
	v_cvt_f32_u32_e32 v4, v1
	s_waitcnt vmcnt(0)
	v_readfirstlane_b32 s4, v3
	s_add_u32 s6, s90, 0x3500
	s_addc_u32 s7, s91, 0
	v_rcp_iflag_f32_e32 v4, v4
	v_add_u32_e32 v2, s4, v2
	v_add_u32_e32 v5, 1, v2
	s_mov_b64 s[8:9], -1
	v_mul_f32_e32 v3, 0x4f7ffffe, v4
	v_cvt_u32_f32_e32 v3, v3
	v_sub_u32_e32 v4, 0, v1
	v_mul_lo_u32 v4, v4, v3
	v_mul_hi_u32 v4, v3, v4
	v_add_u32_e32 v3, v3, v4
	v_mul_hi_u32 v3, v2, v3
	v_mul_lo_u32 v4, v3, v1
	v_sub_u32_e32 v2, v2, v4
	v_add_u32_e32 v6, 1, v3
	v_cmp_ge_u32_e32 vcc, v2, v1
	v_sub_u32_e32 v4, v2, v1
	s_nop 0
	v_cndmask_b32_e32 v3, v3, v6, vcc
	v_cndmask_b32_e32 v2, v2, v4, vcc
	v_add_u32_e32 v4, 1, v3
	v_cmp_ge_u32_e32 vcc, v2, v1
	s_nop 1
	v_cndmask_b32_e32 v4, v3, v4, vcc
	v_mul_lo_u32 v2, v1, v4
	v_add_u32_e32 v1, v2, v1
	v_cmp_ne_u32_e32 vcc, v5, v1
	v_mov_b64_e32 v[2:3], s[6:7]
	s_and_saveexec_b64 s[4:5], vcc
	s_cbranch_execz .LBB0_170
	v_mov_b32_e32 v7, v1
	v_mov_b32_e32 v1, 0
	global_load_dword v2, v1, s[6:7] offset:-256 sc1
	s_mov_b64 s[14:15], 0
	s_waitcnt vmcnt(0)
	v_cmp_lt_u32_e32 vcc, v2, v7
	s_and_saveexec_b64 s[12:13], vcc
	s_cbranch_execz .LBB0_169
	s_add_u32 s8, s90, 0x200
	s_addc_u32 s9, s91, 0
	s_mov_b32 s24, 1
	s_branch .LBB0_162

; __device__ __forceinline__ unsigned xb_ld(unsigned* p)              { return __hip_atomic_load(p, __ATOMIC_RELAXED, __HIP_MEMORY_SCOPE_AGENT); }
; __device__ __forceinline__ unsigned xb_add(unsigned* p, unsigned v) { return __hip_atomic_fetch_add(p, v, __ATOMIC_RELAXED, __HIP_MEMORY_SCOPE_AGENT); }
; #define XB_SPIN(cond, bar) do { unsigned _sp = 0; while (cond) { __builtin_amdgcn_s_sleep(1); \
;     if ((++_sp & 255u) == 0u) { if (xb_ld(&(bar)[XB_TMO])) break; if (_sp > XB_SPIN_CAP) { atomicAdd(&(bar)[XB_TMO], 1u); break; } } } } while (0)
; __device__ __forceinline__ void xcd_barrier(const XcdBarrier& b) {
;     ...
;             const unsigned og = xb_add(&bar[XB_TOP], 1u);
;             const unsigned tg = og / nx;
;             if (og + 1u == (tg + 1u) * nx) xb_add(&bar[XB_TOPGEN], 1u);
;             else XB_SPIN(xb_ld(&bar[XB_TOPGEN]) == tg, bar);
.LBB0_164:
	global_load_dword v2, v1, s[6:7] offset:-256 sc1
	s_add_i32 s24, s24, 1
	s_mov_b64 s[18:19], -1
	s_waitcnt vmcnt(0)
	v_cmp_ge_u32_e32 vcc, v2, v7
	s_orn2_b64 s[22:23], vcc, exec
	s_branch .LBB0_161

; __device__ __forceinline__ unsigned xb_ld(unsigned* p)              { return __hip_atomic_load(p, __ATOMIC_RELAXED, __HIP_MEMORY_SCOPE_AGENT); }
; __device__ __forceinline__ unsigned xb_add(unsigned* p, unsigned v) { return __hip_atomic_fetch_add(p, v, __ATOMIC_RELAXED, __HIP_MEMORY_SCOPE_AGENT); }
; #define XB_SPIN(cond, bar) do { unsigned _sp = 0; while (cond) { __builtin_amdgcn_s_sleep(1); \
;     if ((++_sp & 255u) == 0u) { if (xb_ld(&(bar)[XB_TMO])) break; if (_sp > XB_SPIN_CAP) { atomicAdd(&(bar)[XB_TMO], 1u); break; } } } } while (0)
; __device__ __forceinline__ void xcd_barrier(const XcdBarrier& b) {
;     ...
;         const unsigned old = xb_add(&bar[XB_XSUB(b.x)], 1u);
;         const unsigned gen = old / nloc;
;         if (old + 1u == (gen + 1u) * nloc) {
;             __builtin_amdgcn_fence(__ATOMIC_RELEASE, "agent");
;             asm volatile("s_waitcnt vmcnt(0)" ::: "memory");
;             const unsigned og = xb_add(&bar[XB_TOP], 1u);
;             const unsigned tg = og / nx;
;             if (og + 1u == (tg + 1u) * nx) xb_add(&bar[XB_TOPGEN], 1u);
;             else XB_SPIN(xb_ld(&bar[XB_TOPGEN]) == tg, bar);
.LBB0_258:
	s_or_b64 exec, exec, s[14:15]
	buffer_inv sc1
	v_cvt_f32_u32_e32 v4, v1
	s_waitcnt vmcnt(0)
	v_readfirstlane_b32 s12, v3
	s_add_u32 s14, s90, 0x3500
	s_addc_u32 s15, s91, 0
	v_rcp_iflag_f32_e32 v4, v4
	v_add_u32_e32 v2, s12, v2
	v_add_u32_e32 v5, 1, v2
	s_mov_b64 s[16:17], -1
	v_mul_f32_e32 v3, 0x4f7ffffe, v4
	v_cvt_u32_f32_e32 v3, v3
	v_sub_u32_e32 v4, 0, v1
	v_mul_lo_u32 v4, v4, v3
	v_mul_hi_u32 v4, v3, v4
	v_add_u32_e32 v3, v3, v4
	v_mul_hi_u32 v3, v2, v3
	v_mul_lo_u32 v4, v3, v1
	v_sub_u32_e32 v2, v2, v4
	v_add_u32_e32 v6, 1, v3
	v_cmp_ge_u32_e32 vcc, v2, v1
	v_sub_u32_e32 v4, v2, v1
	s_nop 0
	v_cndmask_b32_e32 v3, v3, v6, vcc
	v_cndmask_b32_e32 v2, v2, v4, vcc
	v_add_u32_e32 v4, 1, v3
	v_cmp_ge_u32_e32 vcc, v2, v1
	s_nop 1
	v_cndmask_b32_e32 v4, v3, v4, vcc
	v_mul_lo_u32 v2, v1, v4
	v_add_u32_e32 v1, v2, v1
	v_cmp_ne_u32_e32 vcc, v5, v1
	v_mov_b64_e32 v[2:3], s[14:15]
	s_and_saveexec_b64 s[12:13], vcc
	s_cbranch_execz .LBB0_270
	v_mov_b32_e32 v7, v1
	v_mov_b32_e32 v1, 0
	global_load_dword v2, v1, s[14:15] offset:-256 sc1
	s_mov_b64 s[20:21], 0
	s_waitcnt vmcnt(0)
	v_cmp_lt_u32_e32 vcc, v2, v7
	s_and_saveexec_b64 s[18:19], vcc
	s_cbranch_execz .LBB0_269
	s_add_u32 s16, s90, 0x200
	s_addc_u32 s17, s91, 0
	s_mov_b32 s30, 1
	s_branch .LBB0_262

; __device__ __forceinline__ unsigned xb_ld(unsigned* p)              { return __hip_atomic_load(p, __ATOMIC_RELAXED, __HIP_MEMORY_SCOPE_AGENT); }
; #define XB_SPIN(cond, bar) do { unsigned _sp = 0; while (cond) { __builtin_amdgcn_s_sleep(1); \
;     if ((++_sp & 255u) == 0u) { if (xb_ld(&(bar)[XB_TMO])) break; if (_sp > XB_SPIN_CAP) { atomicAdd(&(bar)[XB_TMO], 1u); break; } } } } while (0)
; __device__ __forceinline__ void xcd_barrier(const XcdBarrier& b) {
;     ...
;             else XB_SPIN(xb_ld(&bar[XB_TOPGEN]) == tg, bar);
.LBB0_264:
	global_load_dword v2, v1, s[14:15] offset:-256 sc1
	s_add_i32 s30, s30, 1
	s_mov_b64 s[24:25], -1
	s_waitcnt vmcnt(0)
	v_cmp_ge_u32_e32 vcc, v2, v7
	s_orn2_b64 s[28:29], vcc, exec
	s_branch .LBB0_261

; __device__ __forceinline__ unsigned xb_ld(unsigned* p)              { return __hip_atomic_load(p, __ATOMIC_RELAXED, __HIP_MEMORY_SCOPE_AGENT); }
; __device__ __forceinline__ unsigned xb_add(unsigned* p, unsigned v) { return __hip_atomic_fetch_add(p, v, __ATOMIC_RELAXED, __HIP_MEMORY_SCOPE_AGENT); }
; #define XB_SPIN(cond, bar) do { unsigned _sp = 0; while (cond) { __builtin_amdgcn_s_sleep(1); \
;     if ((++_sp & 255u) == 0u) { if (xb_ld(&(bar)[XB_TMO])) break; if (_sp > XB_SPIN_CAP) { atomicAdd(&(bar)[XB_TMO], 1u); break; } } } } while (0)
; __device__ __forceinline__ void xcd_barrier(const XcdBarrier& b) {
;     ...
;         const unsigned old = xb_add(&bar[XB_XSUB(b.x)], 1u);
;         const unsigned gen = old / nloc;
;         if (old + 1u == (gen + 1u) * nloc) {
;             __builtin_amdgcn_fence(__ATOMIC_RELEASE, "agent");
;             asm volatile("s_waitcnt vmcnt(0)" ::: "memory");
;             const unsigned og = xb_add(&bar[XB_TOP], 1u);
;             const unsigned tg = og / nx;
;             if (og + 1u == (tg + 1u) * nx) xb_add(&bar[XB_TOPGEN], 1u);
;             else XB_SPIN(xb_ld(&bar[XB_TOPGEN]) == tg, bar);
.LBB0_678:
	s_or_b64 exec, exec, s[6:7]
	buffer_inv sc1
	v_cvt_f32_u32_e32 v4, v1
	s_waitcnt vmcnt(0)
	v_readfirstlane_b32 s4, v3
	s_add_u32 s6, s90, 0x3500
	s_addc_u32 s7, s91, 0
	v_rcp_iflag_f32_e32 v4, v4
	v_add_u32_e32 v2, s4, v2
	v_add_u32_e32 v5, 1, v2
	s_mov_b64 s[8:9], -1
	v_mul_f32_e32 v3, 0x4f7ffffe, v4
	v_cvt_u32_f32_e32 v3, v3
	v_sub_u32_e32 v4, 0, v1
	v_mul_lo_u32 v4, v4, v3
	v_mul_hi_u32 v4, v3, v4
	v_add_u32_e32 v3, v3, v4
	v_mul_hi_u32 v3, v2, v3
	v_mul_lo_u32 v4, v3, v1
	v_sub_u32_e32 v2, v2, v4
	v_add_u32_e32 v6, 1, v3
	v_cmp_ge_u32_e32 vcc, v2, v1
	v_sub_u32_e32 v4, v2, v1
	s_nop 0
	v_cndmask_b32_e32 v3, v3, v6, vcc
	v_cndmask_b32_e32 v2, v2, v4, vcc
	v_add_u32_e32 v4, 1, v3
	v_cmp_ge_u32_e32 vcc, v2, v1
	s_nop 1
	v_cndmask_b32_e32 v4, v3, v4, vcc
	v_mul_lo_u32 v2, v1, v4
	v_add_u32_e32 v1, v2, v1
	v_cmp_ne_u32_e32 vcc, v5, v1
	v_mov_b64_e32 v[2:3], s[6:7]
	s_and_saveexec_b64 s[4:5], vcc
	s_cbranch_execz .LBB0_690
	v_mov_b32_e32 v7, v1
	v_mov_b32_e32 v1, 0
	global_load_dword v2, v1, s[6:7] offset:-256 sc1
	s_mov_b64 s[12:13], 0
	s_waitcnt vmcnt(0)
	v_cmp_lt_u32_e32 vcc, v2, v7
	s_and_saveexec_b64 s[10:11], vcc
	s_cbranch_execz .LBB0_689
	s_add_u32 s8, s90, 0x200
	s_addc_u32 s9, s91, 0
	s_mov_b32 s22, 1
	s_branch .LBB0_682

; __device__ __forceinline__ unsigned xb_ld(unsigned* p)              { return __hip_atomic_load(p, __ATOMIC_RELAXED, __HIP_MEMORY_SCOPE_AGENT); }
; #define XB_SPIN(cond, bar) do { unsigned _sp = 0; while (cond) { __builtin_amdgcn_s_sleep(1); \
;     if ((++_sp & 255u) == 0u) { if (xb_ld(&(bar)[XB_TMO])) break; if (_sp > XB_SPIN_CAP) { atomicAdd(&(bar)[XB_TMO], 1u); break; } } } } while (0)
; __device__ __forceinline__ void xcd_barrier(const XcdBarrier& b) {
;     ...
;             else XB_SPIN(xb_ld(&bar[XB_TOPGEN]) == tg, bar);
.LBB0_684:
	global_load_dword v2, v1, s[6:7] offset:-256 sc1
	s_add_i32 s22, s22, 1
	s_mov_b64 s[16:17], -1
	s_waitcnt vmcnt(0)
	v_cmp_ge_u32_e32 vcc, v2, v7
	s_orn2_b64 s[20:21], vcc, exec
	s_branch .LBB0_681

; __device__ __forceinline__ unsigned xb_ld(unsigned* p)              { return __hip_atomic_load(p, __ATOMIC_RELAXED, __HIP_MEMORY_SCOPE_AGENT); }
; __device__ __forceinline__ unsigned xb_add(unsigned* p, unsigned v) { return __hip_atomic_fetch_add(p, v, __ATOMIC_RELAXED, __HIP_MEMORY_SCOPE_AGENT); }
; #define XB_SPIN(cond, bar) do { unsigned _sp = 0; while (cond) { __builtin_amdgcn_s_sleep(1); \
;     if ((++_sp & 255u) == 0u) { if (xb_ld(&(bar)[XB_TMO])) break; if (_sp > XB_SPIN_CAP) { atomicAdd(&(bar)[XB_TMO], 1u); break; } } } } while (0)
; __device__ __forceinline__ void xcd_barrier(const XcdBarrier& b) {
;     ...
;         const unsigned old = xb_add(&bar[XB_XSUB(b.x)], 1u);
;         const unsigned gen = old / nloc;
;         if (old + 1u == (gen + 1u) * nloc) {
;             __builtin_amdgcn_fence(__ATOMIC_RELEASE, "agent");
;             asm volatile("s_waitcnt vmcnt(0)" ::: "memory");
;             const unsigned og = xb_add(&bar[XB_TOP], 1u);
;             const unsigned tg = og / nx;
;             if (og + 1u == (tg + 1u) * nx) xb_add(&bar[XB_TOPGEN], 1u);
;             else XB_SPIN(xb_ld(&bar[XB_TOPGEN]) == tg, bar);
.LBB0_1229:
	s_or_b64 exec, exec, s[8:9]
	buffer_inv sc1
	v_cvt_f32_u32_e32 v4, v1
	s_waitcnt vmcnt(0)
	v_readfirstlane_b32 s6, v3
	s_add_u32 s8, s90, 0x3500
	s_addc_u32 s9, s91, 0
	v_rcp_iflag_f32_e32 v4, v4
	v_add_u32_e32 v2, s6, v2
	v_add_u32_e32 v5, 1, v2
	s_mov_b64 s[10:11], -1
	v_mul_f32_e32 v3, 0x4f7ffffe, v4
	v_cvt_u32_f32_e32 v3, v3
	v_sub_u32_e32 v4, 0, v1
	v_mul_lo_u32 v4, v4, v3
	v_mul_hi_u32 v4, v3, v4
	v_add_u32_e32 v3, v3, v4
	v_mul_hi_u32 v3, v2, v3
	v_mul_lo_u32 v4, v3, v1
	v_sub_u32_e32 v2, v2, v4
	v_add_u32_e32 v6, 1, v3
	v_cmp_ge_u32_e32 vcc, v2, v1
	v_sub_u32_e32 v4, v2, v1
	s_nop 0
	v_cndmask_b32_e32 v3, v3, v6, vcc
	v_cndmask_b32_e32 v2, v2, v4, vcc
	v_add_u32_e32 v4, 1, v3
	v_cmp_ge_u32_e32 vcc, v2, v1
	s_nop 1
	v_cndmask_b32_e32 v4, v3, v4, vcc
	v_mul_lo_u32 v2, v1, v4
	v_add_u32_e32 v1, v2, v1
	v_cmp_ne_u32_e32 vcc, v5, v1
	v_mov_b64_e32 v[2:3], s[8:9]
	s_and_saveexec_b64 s[6:7], vcc
	s_cbranch_execz .LBB0_1241
	v_mov_b32_e32 v7, v1
	v_mov_b32_e32 v1, 0
	global_load_dword v2, v1, s[8:9] offset:-256 sc1
	s_mov_b64 s[14:15], 0
	s_waitcnt vmcnt(0)
	v_cmp_lt_u32_e32 vcc, v2, v7
	s_and_saveexec_b64 s[12:13], vcc
	s_cbranch_execz .LBB0_1240
	s_add_u32 s10, s90, 0x200
	s_addc_u32 s11, s91, 0
	s_mov_b32 s24, 1
	s_branch .LBB0_1233

; __device__ __forceinline__ unsigned xb_ld(unsigned* p)              { return __hip_atomic_load(p, __ATOMIC_RELAXED, __HIP_MEMORY_SCOPE_AGENT); }
; #define XB_SPIN(cond, bar) do { unsigned _sp = 0; while (cond) { __builtin_amdgcn_s_sleep(1); \
;     if ((++_sp & 255u) == 0u) { if (xb_ld(&(bar)[XB_TMO])) break; if (_sp > XB_SPIN_CAP) { atomicAdd(&(bar)[XB_TMO], 1u); break; } } } } while (0)
; __device__ __forceinline__ void xcd_barrier(const XcdBarrier& b) {
;     ...
;             else XB_SPIN(xb_ld(&bar[XB_TOPGEN]) == tg, bar);
.LBB0_1235:
	global_load_dword v2, v1, s[8:9] offset:-256 sc1
	s_add_i32 s24, s24, 1
	s_mov_b64 s[18:19], -1
	s_waitcnt vmcnt(0)
	v_cmp_ge_u32_e32 vcc, v2, v7
	s_orn2_b64 s[22:23], vcc, exec
	s_branch .LBB0_1232

; __device__ __forceinline__ unsigned xb_ld(unsigned* p)              { return __hip_atomic_load(p, __ATOMIC_RELAXED, __HIP_MEMORY_SCOPE_AGENT); }
; __device__ __forceinline__ unsigned xb_add(unsigned* p, unsigned v) { return __hip_atomic_fetch_add(p, v, __ATOMIC_RELAXED, __HIP_MEMORY_SCOPE_AGENT); }
; #define XB_SPIN(cond, bar) do { unsigned _sp = 0; while (cond) { __builtin_amdgcn_s_sleep(1); \
;     if ((++_sp & 255u) == 0u) { if (xb_ld(&(bar)[XB_TMO])) break; if (_sp > XB_SPIN_CAP) { atomicAdd(&(bar)[XB_TMO], 1u); break; } } } } while (0)
; __device__ __forceinline__ void xcd_barrier(const XcdBarrier& b) {
;     ...
;         const unsigned old = xb_add(&bar[XB_XSUB(b.x)], 1u);
;         const unsigned gen = old / nloc;
;         if (old + 1u == (gen + 1u) * nloc) {
;             __builtin_amdgcn_fence(__ATOMIC_RELEASE, "agent");
;             asm volatile("s_waitcnt vmcnt(0)" ::: "memory");
;             const unsigned og = xb_add(&bar[XB_TOP], 1u);
;             const unsigned tg = og / nx;
;             if (og + 1u == (tg + 1u) * nx) xb_add(&bar[XB_TOPGEN], 1u);
;             else XB_SPIN(xb_ld(&bar[XB_TOPGEN]) == tg, bar);
.LBB0_1453:
	s_or_b64 exec, exec, s[8:9]
	buffer_inv sc1
	v_cvt_f32_u32_e32 v4, v1
	s_waitcnt vmcnt(0)
	v_readfirstlane_b32 s6, v3
	s_add_u32 s8, s90, 0x3500
	s_addc_u32 s9, s91, 0
	v_rcp_iflag_f32_e32 v4, v4
	v_add_u32_e32 v2, s6, v2
	v_add_u32_e32 v5, 1, v2
	s_mov_b64 s[10:11], -1
	v_mul_f32_e32 v3, 0x4f7ffffe, v4
	v_cvt_u32_f32_e32 v3, v3
	v_sub_u32_e32 v4, 0, v1
	v_mul_lo_u32 v4, v4, v3
	v_mul_hi_u32 v4, v3, v4
	v_add_u32_e32 v3, v3, v4
	v_mul_hi_u32 v3, v2, v3
	v_mul_lo_u32 v4, v3, v1
	v_sub_u32_e32 v2, v2, v4
	v_add_u32_e32 v6, 1, v3
	v_cmp_ge_u32_e32 vcc, v2, v1
	v_sub_u32_e32 v4, v2, v1
	s_nop 0
	v_cndmask_b32_e32 v3, v3, v6, vcc
	v_cndmask_b32_e32 v2, v2, v4, vcc
	v_add_u32_e32 v4, 1, v3
	v_cmp_ge_u32_e32 vcc, v2, v1
	s_nop 1
	v_cndmask_b32_e32 v4, v3, v4, vcc
	v_mul_lo_u32 v2, v1, v4
	v_add_u32_e32 v1, v2, v1
	v_cmp_ne_u32_e32 vcc, v5, v1
	v_mov_b64_e32 v[2:3], s[8:9]
	s_and_saveexec_b64 s[6:7], vcc
	s_cbranch_execz .LBB0_1465
	v_mov_b32_e32 v7, v1
	v_mov_b32_e32 v1, 0
	global_load_dword v2, v1, s[8:9] offset:-256 sc1
	s_mov_b64 s[24:25], 0
	s_waitcnt vmcnt(0)
	v_cmp_lt_u32_e32 vcc, v2, v7
	s_and_saveexec_b64 s[12:13], vcc
	s_cbranch_execz .LBB0_1464
	s_add_u32 s10, s90, 0x200
	s_addc_u32 s11, s91, 0
	s_mov_b32 s22, 1
	s_branch .LBB0_1457

; __device__ __forceinline__ unsigned xb_ld(unsigned* p)              { return __hip_atomic_load(p, __ATOMIC_RELAXED, __HIP_MEMORY_SCOPE_AGENT); }
; #define XB_SPIN(cond, bar) do { unsigned _sp = 0; while (cond) { __builtin_amdgcn_s_sleep(1); \
;     if ((++_sp & 255u) == 0u) { if (xb_ld(&(bar)[XB_TMO])) break; if (_sp > XB_SPIN_CAP) { atomicAdd(&(bar)[XB_TMO], 1u); break; } } } } while (0)
; __device__ __forceinline__ void xcd_barrier(const XcdBarrier& b) {
;     ...
;             else XB_SPIN(xb_ld(&bar[XB_TOPGEN]) == tg, bar);
.LBB0_1459:
	global_load_dword v2, v1, s[8:9] offset:-256 sc1
	s_add_i32 s22, s22, 1
	s_mov_b64 s[28:29], -1
	s_waitcnt vmcnt(0)
	v_cmp_ge_u32_e32 vcc, v2, v7
	s_orn2_b64 s[34:35], vcc, exec
	s_branch .LBB0_1456

; __device__ __forceinline__ unsigned xb_ld(unsigned* p)              { return __hip_atomic_load(p, __ATOMIC_RELAXED, __HIP_MEMORY_SCOPE_AGENT); }
; __device__ __forceinline__ unsigned xb_add(unsigned* p, unsigned v) { return __hip_atomic_fetch_add(p, v, __ATOMIC_RELAXED, __HIP_MEMORY_SCOPE_AGENT); }
; #define XB_SPIN(cond, bar) do { unsigned _sp = 0; while (cond) { __builtin_amdgcn_s_sleep(1); \
;     if ((++_sp & 255u) == 0u) { if (xb_ld(&(bar)[XB_TMO])) break; if (_sp > XB_SPIN_CAP) { atomicAdd(&(bar)[XB_TMO], 1u); break; } } } } while (0)
; __device__ __forceinline__ void xcd_barrier(const XcdBarrier& b) {
;     ...
;         const unsigned old = xb_add(&bar[XB_XSUB(b.x)], 1u);
;         const unsigned gen = old / nloc;
;         if (old + 1u == (gen + 1u) * nloc) {
;             __builtin_amdgcn_fence(__ATOMIC_RELEASE, "agent");
;             asm volatile("s_waitcnt vmcnt(0)" ::: "memory");
;             const unsigned og = xb_add(&bar[XB_TOP], 1u);
;             const unsigned tg = og / nx;
;             if (og + 1u == (tg + 1u) * nx) xb_add(&bar[XB_TOPGEN], 1u);
;             else XB_SPIN(xb_ld(&bar[XB_TOPGEN]) == tg, bar);
.LBB0_1760:
	s_or_b64 exec, exec, s[8:9]
	buffer_inv sc1
	v_cvt_f32_u32_e32 v4, v1
	s_waitcnt vmcnt(0)
	v_readfirstlane_b32 s6, v3
	s_add_u32 s8, s90, 0x3500
	s_addc_u32 s9, s91, 0
	v_rcp_iflag_f32_e32 v4, v4
	v_add_u32_e32 v2, s6, v2
	v_add_u32_e32 v5, 1, v2
	s_mov_b64 s[10:11], -1
	v_mul_f32_e32 v3, 0x4f7ffffe, v4
	v_cvt_u32_f32_e32 v3, v3
	v_sub_u32_e32 v4, 0, v1
	v_mul_lo_u32 v4, v4, v3
	v_mul_hi_u32 v4, v3, v4
	v_add_u32_e32 v3, v3, v4
	v_mul_hi_u32 v3, v2, v3
	v_mul_lo_u32 v4, v3, v1
	v_sub_u32_e32 v2, v2, v4
	v_add_u32_e32 v6, 1, v3
	v_cmp_ge_u32_e32 vcc, v2, v1
	v_sub_u32_e32 v4, v2, v1
	s_nop 0
	v_cndmask_b32_e32 v3, v3, v6, vcc
	v_cndmask_b32_e32 v2, v2, v4, vcc
	v_add_u32_e32 v4, 1, v3
	v_cmp_ge_u32_e32 vcc, v2, v1
	s_nop 1
	v_cndmask_b32_e32 v4, v3, v4, vcc
	v_mul_lo_u32 v2, v1, v4
	v_add_u32_e32 v1, v2, v1
	v_cmp_ne_u32_e32 vcc, v5, v1
	v_mov_b64_e32 v[2:3], s[8:9]
	s_and_saveexec_b64 s[6:7], vcc
	s_cbranch_execz .LBB0_1772
	v_mov_b32_e32 v7, v1
	v_mov_b32_e32 v1, 0
	global_load_dword v2, v1, s[8:9] offset:-256 sc1
	s_mov_b64 s[14:15], 0
	s_waitcnt vmcnt(0)
	v_cmp_lt_u32_e32 vcc, v2, v7
	s_and_saveexec_b64 s[12:13], vcc
	s_cbranch_execz .LBB0_1771
	s_add_u32 s10, s90, 0x200
	s_addc_u32 s11, s91, 0
	s_mov_b32 s28, 1
	s_branch .LBB0_1764

; __device__ __forceinline__ unsigned xb_ld(unsigned* p)              { return __hip_atomic_load(p, __ATOMIC_RELAXED, __HIP_MEMORY_SCOPE_AGENT); }
; #define XB_SPIN(cond, bar) do { unsigned _sp = 0; while (cond) { __builtin_amdgcn_s_sleep(1); \
;     if ((++_sp & 255u) == 0u) { if (xb_ld(&(bar)[XB_TMO])) break; if (_sp > XB_SPIN_CAP) { atomicAdd(&(bar)[XB_TMO], 1u); break; } } } } while (0)
; __device__ __forceinline__ void xcd_barrier(const XcdBarrier& b) {
;     ...
;             else XB_SPIN(xb_ld(&bar[XB_TOPGEN]) == tg, bar);
.LBB0_1766:
	global_load_dword v2, v1, s[8:9] offset:-256 sc1
	s_add_i32 s28, s28, 1
	s_mov_b64 s[22:23], -1
	s_waitcnt vmcnt(0)
	v_cmp_ge_u32_e32 vcc, v2, v7
	s_orn2_b64 s[26:27], vcc, exec
	s_branch .LBB0_1763

; __device__ __forceinline__ unsigned xb_ld(unsigned* p)              { return __hip_atomic_load(p, __ATOMIC_RELAXED, __HIP_MEMORY_SCOPE_AGENT); }
; __device__ __forceinline__ unsigned xb_add(unsigned* p, unsigned v) { return __hip_atomic_fetch_add(p, v, __ATOMIC_RELAXED, __HIP_MEMORY_SCOPE_AGENT); }
; #define XB_SPIN(cond, bar) do { unsigned _sp = 0; while (cond) { __builtin_amdgcn_s_sleep(1); \
;     if ((++_sp & 255u) == 0u) { if (xb_ld(&(bar)[XB_TMO])) break; if (_sp > XB_SPIN_CAP) { atomicAdd(&(bar)[XB_TMO], 1u); break; } } } } while (0)
; __device__ __forceinline__ void xcd_barrier(const XcdBarrier& b) {
;     ...
;         const unsigned old = xb_add(&bar[XB_XSUB(b.x)], 1u);
;         const unsigned gen = old / nloc;
;         if (old + 1u == (gen + 1u) * nloc) {
;             __builtin_amdgcn_fence(__ATOMIC_RELEASE, "agent");
;             asm volatile("s_waitcnt vmcnt(0)" ::: "memory");
;             const unsigned og = xb_add(&bar[XB_TOP], 1u);
;             const unsigned tg = og / nx;
;             if (og + 1u == (tg + 1u) * nx) xb_add(&bar[XB_TOPGEN], 1u);
;             else XB_SPIN(xb_ld(&bar[XB_TOPGEN]) == tg, bar);
.LBB0_1843:
	s_or_b64 exec, exec, s[8:9]
	buffer_inv sc1
	v_cvt_f32_u32_e32 v4, v1
	s_waitcnt vmcnt(0)
	v_readfirstlane_b32 s6, v3
	s_add_u32 s8, s90, 0x3500
	s_addc_u32 s9, s91, 0
	v_rcp_iflag_f32_e32 v4, v4
	v_add_u32_e32 v2, s6, v2
	v_add_u32_e32 v5, 1, v2
	s_mov_b64 s[10:11], -1
	v_mul_f32_e32 v3, 0x4f7ffffe, v4
	v_cvt_u32_f32_e32 v3, v3
	v_sub_u32_e32 v4, 0, v1
	v_mul_lo_u32 v4, v4, v3
	v_mul_hi_u32 v4, v3, v4
	v_add_u32_e32 v3, v3, v4
	v_mul_hi_u32 v3, v2, v3
	v_mul_lo_u32 v4, v3, v1
	v_sub_u32_e32 v2, v2, v4
	v_add_u32_e32 v6, 1, v3
	v_cmp_ge_u32_e32 vcc, v2, v1
	v_sub_u32_e32 v4, v2, v1
	s_nop 0
	v_cndmask_b32_e32 v3, v3, v6, vcc
	v_cndmask_b32_e32 v2, v2, v4, vcc
	v_add_u32_e32 v4, 1, v3
	v_cmp_ge_u32_e32 vcc, v2, v1
	s_nop 1
	v_cndmask_b32_e32 v4, v3, v4, vcc
	v_mul_lo_u32 v2, v1, v4
	v_add_u32_e32 v1, v2, v1
	v_cmp_ne_u32_e32 vcc, v5, v1
	v_mov_b64_e32 v[2:3], s[8:9]
	s_and_saveexec_b64 s[6:7], vcc
	s_cbranch_execz .LBB0_1855
	v_mov_b32_e32 v7, v1
	v_mov_b32_e32 v1, 0
	global_load_dword v2, v1, s[8:9] offset:-256 sc1
	s_mov_b64 s[14:15], 0
	s_waitcnt vmcnt(0)
	v_cmp_lt_u32_e32 vcc, v2, v7
	s_and_saveexec_b64 s[12:13], vcc
	s_cbranch_execz .LBB0_1854
	s_add_u32 s10, s90, 0x200
	s_addc_u32 s11, s91, 0
	s_mov_b32 s26, 1
	s_branch .LBB0_1847

; __device__ __forceinline__ unsigned xb_ld(unsigned* p)              { return __hip_atomic_load(p, __ATOMIC_RELAXED, __HIP_MEMORY_SCOPE_AGENT); }
; #define XB_SPIN(cond, bar) do { unsigned _sp = 0; while (cond) { __builtin_amdgcn_s_sleep(1); \
;     if ((++_sp & 255u) == 0u) { if (xb_ld(&(bar)[XB_TMO])) break; if (_sp > XB_SPIN_CAP) { atomicAdd(&(bar)[XB_TMO], 1u); break; } } } } while (0)
; __device__ __forceinline__ void xcd_barrier(const XcdBarrier& b) {
;     ...
;             else XB_SPIN(xb_ld(&bar[XB_TOPGEN]) == tg, bar);
.LBB0_1849:
	global_load_dword v2, v1, s[8:9] offset:-256 sc1
	s_add_i32 s26, s26, 1
	s_mov_b64 s[20:21], -1
	s_waitcnt vmcnt(0)
	v_cmp_ge_u32_e32 vcc, v2, v7
	s_orn2_b64 s[24:25], vcc, exec
	s_branch .LBB0_1846
